# lora phase: LIN tile staging loop unrolled (7 loads in flight, one wait) instead of load-wait-ds_write per iteration
# speedup vs baseline: 1.0148x; 1.0070x over previous
.LBB0_977:
	s_mov_b32 s2, 0x92492493
	v_mul_hi_i32 v5, v4, s2
	v_add_u32_e32 v5, v5, v4
	v_lshrrev_b32_e32 v6, 31, v5
	v_ashrrev_i32_e32 v5, 5, v5
	v_add_u32_e32 v10, v5, v6
	v_ashrrev_i32_e32 v11, 31, v10
	v_lshl_add_u64 v[6:7], s[18:19], 0, v[10:11]
	v_mov_b64_e32 v[8:9], s[14:15]
	v_mad_u64_u32 v[8:9], s[24:25], v6, s9, v[8:9]
	s_movk_i32 s2, 0xfe40
	v_mad_i32_i24 v9, v7, s9, v9
	v_mad_u64_u32 v[6:7], s[24:25], v10, s2, v[2:3]
	v_ashrrev_i32_e32 v7, 31, v6
	v_lshl_add_u64 v[6:7], v[6:7], 1, v[8:9]
	global_load_dwordx4 v[180:183], v[6:7], off
	v_lshl_add_u32 v184, v10, 4, v3
	v_add_u32_e32 v3, 0x2000, v3
	v_add_u32_e32 v2, 0x1000, v2
	v_add_u32_e32 v5, 0x200, v4
	v_mov_b32_e32 v4, v5
	s_mov_b32 s2, 0x92492493
	v_mul_hi_i32 v5, v4, s2
	v_add_u32_e32 v5, v5, v4
	v_lshrrev_b32_e32 v6, 31, v5
	v_ashrrev_i32_e32 v5, 5, v5
	v_add_u32_e32 v10, v5, v6
	v_ashrrev_i32_e32 v11, 31, v10
	v_lshl_add_u64 v[6:7], s[18:19], 0, v[10:11]
	v_mov_b64_e32 v[8:9], s[14:15]
	v_mad_u64_u32 v[8:9], s[24:25], v6, s9, v[8:9]
	s_movk_i32 s2, 0xfe40
	v_mad_i32_i24 v9, v7, s9, v9
	v_mad_u64_u32 v[6:7], s[24:25], v10, s2, v[2:3]
	v_ashrrev_i32_e32 v7, 31, v6
	v_lshl_add_u64 v[6:7], v[6:7], 1, v[8:9]
	global_load_dwordx4 v[186:189], v[6:7], off
	v_lshl_add_u32 v190, v10, 4, v3
	v_add_u32_e32 v3, 0x2000, v3
	v_add_u32_e32 v2, 0x1000, v2
	v_add_u32_e32 v5, 0x200, v4
	v_mov_b32_e32 v4, v5
	s_mov_b32 s2, 0x92492493
	v_mul_hi_i32 v5, v4, s2
	v_add_u32_e32 v5, v5, v4
	v_lshrrev_b32_e32 v6, 31, v5
	v_ashrrev_i32_e32 v5, 5, v5
	v_add_u32_e32 v10, v5, v6
	v_ashrrev_i32_e32 v11, 31, v10
	v_lshl_add_u64 v[6:7], s[18:19], 0, v[10:11]
	v_mov_b64_e32 v[8:9], s[14:15]
	v_mad_u64_u32 v[8:9], s[24:25], v6, s9, v[8:9]
	s_movk_i32 s2, 0xfe40
	v_mad_i32_i24 v9, v7, s9, v9
	v_mad_u64_u32 v[6:7], s[24:25], v10, s2, v[2:3]
	v_ashrrev_i32_e32 v7, 31, v6
	v_lshl_add_u64 v[6:7], v[6:7], 1, v[8:9]
	global_load_dwordx4 v[192:195], v[6:7], off
	v_lshl_add_u32 v196, v10, 4, v3
	v_add_u32_e32 v3, 0x2000, v3
	v_add_u32_e32 v2, 0x1000, v2
	v_add_u32_e32 v5, 0x200, v4
	v_mov_b32_e32 v4, v5
	s_mov_b32 s2, 0x92492493
	v_mul_hi_i32 v5, v4, s2
	v_add_u32_e32 v5, v5, v4
	v_lshrrev_b32_e32 v6, 31, v5
	v_ashrrev_i32_e32 v5, 5, v5
	v_add_u32_e32 v10, v5, v6
	v_ashrrev_i32_e32 v11, 31, v10
	v_lshl_add_u64 v[6:7], s[18:19], 0, v[10:11]
	v_mov_b64_e32 v[8:9], s[14:15]
	v_mad_u64_u32 v[8:9], s[24:25], v6, s9, v[8:9]
	s_movk_i32 s2, 0xfe40
	v_mad_i32_i24 v9, v7, s9, v9
	v_mad_u64_u32 v[6:7], s[24:25], v10, s2, v[2:3]
	v_ashrrev_i32_e32 v7, 31, v6
	v_lshl_add_u64 v[6:7], v[6:7], 1, v[8:9]
	global_load_dwordx4 v[198:201], v[6:7], off
	v_lshl_add_u32 v202, v10, 4, v3
	v_add_u32_e32 v3, 0x2000, v3
	v_add_u32_e32 v2, 0x1000, v2
	v_add_u32_e32 v5, 0x200, v4
	v_mov_b32_e32 v4, v5
	s_mov_b32 s2, 0x92492493
	v_mul_hi_i32 v5, v4, s2
	v_add_u32_e32 v5, v5, v4
	v_lshrrev_b32_e32 v6, 31, v5
	v_ashrrev_i32_e32 v5, 5, v5
	v_add_u32_e32 v10, v5, v6
	v_ashrrev_i32_e32 v11, 31, v10
	v_lshl_add_u64 v[6:7], s[18:19], 0, v[10:11]
	v_mov_b64_e32 v[8:9], s[14:15]
	v_mad_u64_u32 v[8:9], s[24:25], v6, s9, v[8:9]
	s_movk_i32 s2, 0xfe40
	v_mad_i32_i24 v9, v7, s9, v9
	v_mad_u64_u32 v[6:7], s[24:25], v10, s2, v[2:3]
	v_ashrrev_i32_e32 v7, 31, v6
	v_lshl_add_u64 v[6:7], v[6:7], 1, v[8:9]
	global_load_dwordx4 v[204:207], v[6:7], off
	v_lshl_add_u32 v208, v10, 4, v3
	v_add_u32_e32 v3, 0x2000, v3
	v_add_u32_e32 v2, 0x1000, v2
	v_add_u32_e32 v5, 0x200, v4
	v_mov_b32_e32 v4, v5
	s_mov_b32 s2, 0x92492493
	v_mul_hi_i32 v5, v4, s2
	v_add_u32_e32 v5, v5, v4
	v_lshrrev_b32_e32 v6, 31, v5
	v_ashrrev_i32_e32 v5, 5, v5
	v_add_u32_e32 v10, v5, v6
	v_ashrrev_i32_e32 v11, 31, v10
	v_lshl_add_u64 v[6:7], s[18:19], 0, v[10:11]
	v_mov_b64_e32 v[8:9], s[14:15]
	v_mad_u64_u32 v[8:9], s[24:25], v6, s9, v[8:9]
	s_movk_i32 s2, 0xfe40
	v_mad_i32_i24 v9, v7, s9, v9
	v_mad_u64_u32 v[6:7], s[24:25], v10, s2, v[2:3]
	v_ashrrev_i32_e32 v7, 31, v6
	v_lshl_add_u64 v[6:7], v[6:7], 1, v[8:9]
	global_load_dwordx4 v[210:213], v[6:7], off
	v_lshl_add_u32 v214, v10, 4, v3
	v_add_u32_e32 v3, 0x2000, v3
	v_add_u32_e32 v2, 0x1000, v2
	v_add_u32_e32 v5, 0x200, v4
	v_mov_b32_e32 v4, v5
	s_mov_b32 s2, 0x92492493
	v_mul_hi_i32 v5, v4, s2
	v_add_u32_e32 v5, v5, v4
	v_lshrrev_b32_e32 v6, 31, v5
	v_ashrrev_i32_e32 v5, 5, v5
	v_add_u32_e32 v10, v5, v6
	v_ashrrev_i32_e32 v11, 31, v10
	v_lshl_add_u64 v[6:7], s[18:19], 0, v[10:11]
	v_mov_b64_e32 v[8:9], s[14:15]
	v_mad_u64_u32 v[8:9], s[24:25], v6, s9, v[8:9]
	s_movk_i32 s2, 0xfe40
	v_mad_i32_i24 v9, v7, s9, v9
	v_mad_u64_u32 v[6:7], s[24:25], v10, s2, v[2:3]
	v_ashrrev_i32_e32 v7, 31, v6
	v_lshl_add_u64 v[6:7], v[6:7], 1, v[8:9]
	global_load_dwordx4 v[216:219], v[6:7], off
	v_lshl_add_u32 v220, v10, 4, v3
	v_add_u32_e32 v3, 0x2000, v3
	v_add_u32_e32 v2, 0x1000, v2
	v_add_u32_e32 v5, 0x200, v4
	v_mov_b32_e32 v4, v5
	s_waitcnt vmcnt(0)
	ds_write_b128 v184, v[180:183]
	ds_write_b128 v190, v[186:189]
	ds_write_b128 v196, v[192:195]
	ds_write_b128 v202, v[198:201]
	ds_write_b128 v208, v[204:207]
	ds_write_b128 v214, v[210:213]
	ds_write_b128 v220, v[216:219]

.LBB0_3295:
	s_mov_b32 s2, 0x92492493
	v_mul_hi_i32 v83, v82, s2
	v_add_u32_e32 v83, v83, v82
	s_waitcnt vmcnt(17)
	v_lshrrev_b32_e32 v84, 31, v83
	v_ashrrev_i32_e32 v83, 5, v83
	v_add_u32_e32 v88, v83, v84
	v_ashrrev_i32_e32 v89, 31, v88
	v_lshl_add_u64 v[84:85], s[22:23], 0, v[88:89]
	s_waitcnt vmcnt(16)
	v_mov_b64_e32 v[86:87], s[18:19]
	v_mad_u64_u32 v[86:87], s[2:3], v84, s7, v[86:87]
	s_movk_i32 s2, 0xfe40
	v_mad_i32_i24 v87, v85, s7, v87
	v_mad_u64_u32 v[84:85], s[2:3], v88, s2, v[80:81]
	v_ashrrev_i32_e32 v85, 31, v84
	v_lshl_add_u64 v[84:85], v[84:85], 1, v[86:87]
	global_load_dwordx4 v[180:183], v[84:85], off
	v_lshl_add_u32 v184, v88, 4, v81
	v_add_u32_e32 v81, 0x2000, v81
	v_add_u32_e32 v80, 0x1000, v80
	v_add_u32_e32 v83, 0x200, v82
	v_mov_b32_e32 v82, v83
	s_mov_b32 s2, 0x92492493
	v_mul_hi_i32 v83, v82, s2
	v_add_u32_e32 v83, v83, v82
	s_waitcnt vmcnt(17)
	v_lshrrev_b32_e32 v84, 31, v83
	v_ashrrev_i32_e32 v83, 5, v83
	v_add_u32_e32 v88, v83, v84
	v_ashrrev_i32_e32 v89, 31, v88
	v_lshl_add_u64 v[84:85], s[22:23], 0, v[88:89]
	s_waitcnt vmcnt(16)
	v_mov_b64_e32 v[86:87], s[18:19]
	v_mad_u64_u32 v[86:87], s[2:3], v84, s7, v[86:87]
	s_movk_i32 s2, 0xfe40
	v_mad_i32_i24 v87, v85, s7, v87
	v_mad_u64_u32 v[84:85], s[2:3], v88, s2, v[80:81]
	v_ashrrev_i32_e32 v85, 31, v84
	v_lshl_add_u64 v[84:85], v[84:85], 1, v[86:87]
	global_load_dwordx4 v[186:189], v[84:85], off
	v_lshl_add_u32 v190, v88, 4, v81
	v_add_u32_e32 v81, 0x2000, v81
	v_add_u32_e32 v80, 0x1000, v80
	v_add_u32_e32 v83, 0x200, v82
	v_mov_b32_e32 v82, v83
	s_mov_b32 s2, 0x92492493
	v_mul_hi_i32 v83, v82, s2
	v_add_u32_e32 v83, v83, v82
	s_waitcnt vmcnt(17)
	v_lshrrev_b32_e32 v84, 31, v83
	v_ashrrev_i32_e32 v83, 5, v83
	v_add_u32_e32 v88, v83, v84
	v_ashrrev_i32_e32 v89, 31, v88
	v_lshl_add_u64 v[84:85], s[22:23], 0, v[88:89]
	s_waitcnt vmcnt(16)
	v_mov_b64_e32 v[86:87], s[18:19]
	v_mad_u64_u32 v[86:87], s[2:3], v84, s7, v[86:87]
	s_movk_i32 s2, 0xfe40
	v_mad_i32_i24 v87, v85, s7, v87
	v_mad_u64_u32 v[84:85], s[2:3], v88, s2, v[80:81]
	v_ashrrev_i32_e32 v85, 31, v84
	v_lshl_add_u64 v[84:85], v[84:85], 1, v[86:87]
	global_load_dwordx4 v[192:195], v[84:85], off
	v_lshl_add_u32 v196, v88, 4, v81
	v_add_u32_e32 v81, 0x2000, v81
	v_add_u32_e32 v80, 0x1000, v80
	v_add_u32_e32 v83, 0x200, v82
	v_mov_b32_e32 v82, v83
	s_mov_b32 s2, 0x92492493
	v_mul_hi_i32 v83, v82, s2
	v_add_u32_e32 v83, v83, v82
	s_waitcnt vmcnt(17)
	v_lshrrev_b32_e32 v84, 31, v83
	v_ashrrev_i32_e32 v83, 5, v83
	v_add_u32_e32 v88, v83, v84
	v_ashrrev_i32_e32 v89, 31, v88
	v_lshl_add_u64 v[84:85], s[22:23], 0, v[88:89]
	s_waitcnt vmcnt(16)
	v_mov_b64_e32 v[86:87], s[18:19]
	v_mad_u64_u32 v[86:87], s[2:3], v84, s7, v[86:87]
	s_movk_i32 s2, 0xfe40
	v_mad_i32_i24 v87, v85, s7, v87
	v_mad_u64_u32 v[84:85], s[2:3], v88, s2, v[80:81]
	v_ashrrev_i32_e32 v85, 31, v84
	v_lshl_add_u64 v[84:85], v[84:85], 1, v[86:87]
	global_load_dwordx4 v[198:201], v[84:85], off
	v_lshl_add_u32 v202, v88, 4, v81
	v_add_u32_e32 v81, 0x2000, v81
	v_add_u32_e32 v80, 0x1000, v80
	v_add_u32_e32 v83, 0x200, v82
	v_mov_b32_e32 v82, v83
	s_mov_b32 s2, 0x92492493
	v_mul_hi_i32 v83, v82, s2
	v_add_u32_e32 v83, v83, v82
	s_waitcnt vmcnt(17)
	v_lshrrev_b32_e32 v84, 31, v83
	v_ashrrev_i32_e32 v83, 5, v83
	v_add_u32_e32 v88, v83, v84
	v_ashrrev_i32_e32 v89, 31, v88
	v_lshl_add_u64 v[84:85], s[22:23], 0, v[88:89]
	s_waitcnt vmcnt(16)
	v_mov_b64_e32 v[86:87], s[18:19]
	v_mad_u64_u32 v[86:87], s[2:3], v84, s7, v[86:87]
	s_movk_i32 s2, 0xfe40
	v_mad_i32_i24 v87, v85, s7, v87
	v_mad_u64_u32 v[84:85], s[2:3], v88, s2, v[80:81]
	v_ashrrev_i32_e32 v85, 31, v84
	v_lshl_add_u64 v[84:85], v[84:85], 1, v[86:87]
	global_load_dwordx4 v[204:207], v[84:85], off
	v_lshl_add_u32 v208, v88, 4, v81
	v_add_u32_e32 v81, 0x2000, v81
	v_add_u32_e32 v80, 0x1000, v80
	v_add_u32_e32 v83, 0x200, v82
	v_mov_b32_e32 v82, v83
	s_mov_b32 s2, 0x92492493
	v_mul_hi_i32 v83, v82, s2
	v_add_u32_e32 v83, v83, v82
	s_waitcnt vmcnt(17)
	v_lshrrev_b32_e32 v84, 31, v83
	v_ashrrev_i32_e32 v83, 5, v83
	v_add_u32_e32 v88, v83, v84
	v_ashrrev_i32_e32 v89, 31, v88
	v_lshl_add_u64 v[84:85], s[22:23], 0, v[88:89]
	s_waitcnt vmcnt(16)
	v_mov_b64_e32 v[86:87], s[18:19]
	v_mad_u64_u32 v[86:87], s[2:3], v84, s7, v[86:87]
	s_movk_i32 s2, 0xfe40
	v_mad_i32_i24 v87, v85, s7, v87
	v_mad_u64_u32 v[84:85], s[2:3], v88, s2, v[80:81]
	v_ashrrev_i32_e32 v85, 31, v84
	v_lshl_add_u64 v[84:85], v[84:85], 1, v[86:87]
	global_load_dwordx4 v[210:213], v[84:85], off
	v_lshl_add_u32 v214, v88, 4, v81
	v_add_u32_e32 v81, 0x2000, v81
	v_add_u32_e32 v80, 0x1000, v80
	v_add_u32_e32 v83, 0x200, v82
	v_mov_b32_e32 v82, v83
	s_mov_b32 s2, 0x92492493
	v_mul_hi_i32 v83, v82, s2
	v_add_u32_e32 v83, v83, v82
	s_waitcnt vmcnt(17)
	v_lshrrev_b32_e32 v84, 31, v83
	v_ashrrev_i32_e32 v83, 5, v83
	v_add_u32_e32 v88, v83, v84
	v_ashrrev_i32_e32 v89, 31, v88
	v_lshl_add_u64 v[84:85], s[22:23], 0, v[88:89]
	s_waitcnt vmcnt(16)
	v_mov_b64_e32 v[86:87], s[18:19]
	v_mad_u64_u32 v[86:87], s[2:3], v84, s7, v[86:87]
	s_movk_i32 s2, 0xfe40
	v_mad_i32_i24 v87, v85, s7, v87
	v_mad_u64_u32 v[84:85], s[2:3], v88, s2, v[80:81]
	v_ashrrev_i32_e32 v85, 31, v84
	v_lshl_add_u64 v[84:85], v[84:85], 1, v[86:87]
	global_load_dwordx4 v[216:219], v[84:85], off
	v_lshl_add_u32 v220, v88, 4, v81
	v_add_u32_e32 v81, 0x2000, v81
	v_add_u32_e32 v80, 0x1000, v80
	v_add_u32_e32 v83, 0x200, v82
	v_mov_b32_e32 v82, v83
	s_waitcnt vmcnt(0)
	ds_write_b128 v184, v[180:183]
	ds_write_b128 v190, v[186:189]
	ds_write_b128 v196, v[192:195]
	ds_write_b128 v202, v[198:201]
	ds_write_b128 v208, v[204:207]
	ds_write_b128 v214, v[210:213]
	ds_write_b128 v220, v[216:219]
